# speedup vs baseline: 1.0074x; 1.0074x over previous
.LBB1_69:
	s_or_b64 exec, exec, s[2:3]
	v_or_b32_e32 v100, v126, v125
	v_add_u32_e32 v104, 16, v100
	v_or_b32_e32 v101, v100, v121
	v_add_u16_e32 v102, v104, v121
	v_lshlrev_b32_e32 v101, 1, v101
	v_lshrrev_b16_e32 v102, 1, v102
	v_and_b32_e32 v101, 0x7fc, v101
	v_lshlrev_b32_e32 v102, 2, v102
	s_waitcnt vmcnt(0)
	s_barrier
	v_mov_b32_e32 v101, v232
	v_lshrrev_b32_e32 v103, 2, v107
	v_mov_b32_e32 v102, v233
	v_bitop3_b32 v108, v126, v124, v125 bitop3:0x36
	v_and_or_b32 v105, v103, 12, v127
	v_lshlrev_b32_e32 v103, 1, v108
	v_add_u32_e32 v108, 32, v100
	v_add_u16_e32 v113, v108, v121
	v_lshrrev_b16_e32 v113, 1, v113
	v_lshlrev_b32_e32 v113, 2, v113
	v_mov_b32_e32 v113, v234
	v_add_u32_e32 v110, 0x60, v100
	v_add_u32_e32 v111, 0x70, v100
	s_movk_i32 s1, 0x180
	v_or_b32_e32 v112, 0x80, v100
	v_mul_lo_u32 v105, v105, s1
	v_xor_b32_e32 v104, v104, v124
	v_add_u16_e32 v114, v110, v121
	v_add_u16_e32 v115, v111, v121
	v_add_u16_e32 v112, v112, v121
	v_add3_u32 v116, 0, v103, v105
	v_lshlrev_b32_e32 v103, 1, v104
	v_lshrrev_b16_e32 v104, 1, v114
	v_lshrrev_b16_e32 v114, 1, v115
	v_lshrrev_b16_e32 v112, 1, v112
	v_add3_u32 v115, 0, v103, v105
	v_lshlrev_b32_e32 v103, 2, v104
	v_lshlrev_b32_e32 v104, 2, v114
	v_lshlrev_b32_e32 v112, 2, v112
	v_mov_b32_e32 v114, v235
	s_nop 0
	v_mov_b32_e32 v104, v236
	s_nop 0
	v_mov_b32_e32 v103, v237
	v_and_b32_e32 v247, 1, v107
	v_cmp_eq_u32_e64 s[12:13], 0, v247
	v_mov_b32_e32 v245, 0x1000504
	v_mov_b32_e32 v247, 0x5040100
	v_cndmask_b32_e64 v245, v245, v247, s[12:13]
	v_mov_b32_e32 v246, 0x3020706
	v_mov_b32_e32 v247, 0x7060302
	v_cndmask_b32_e64 v246, v246, v247, s[12:13]
	v_lshrrev_b32_e32 v247, 7, v107
	v_lshlrev_b32_e32 v247, 5, v247
	v_bfe_u32 v254, v107, 4, 2
	v_lshl_add_u32 v247, v254, 2, v247
	v_mul_u32_u24_e32 v247, 0x180, v247
	v_mov_b32_e32 v244, 0x2fe
	v_cndmask_b32_e64 v244, v244, 0, s[12:13]
	v_add_u32_e32 v247, v247, v244
	v_lshlrev_b32_e32 v254, 4, v254
	v_bfe_u32 v244, v107, 6, 1
	v_mul_u32_u24_e32 v244, 48, v244
	v_and_b32_e32 v248, 15, v107
	v_add_u32_e32 v244, v244, v248
	v_mov_b32_e32 v248, v244
	v_xor_b32_e32 v248, v248, v254
	v_lshl_add_u32 v248, v248, 1, v247
	v_add_u32_e32 v249, 16, v244
	v_xor_b32_e32 v249, v249, v254
	v_lshl_add_u32 v249, v249, 1, v247
	v_add_u32_e32 v250, 32, v244
	v_xor_b32_e32 v250, v250, v254
	v_lshl_add_u32 v250, v250, 1, v247
	v_add_u32_e32 v251, 96, v244
	v_xor_b32_e32 v251, v251, v254
	v_lshl_add_u32 v251, v251, 1, v247
	v_add_u32_e32 v252, 112, v244
	v_xor_b32_e32 v252, v252, v254
	v_lshl_add_u32 v252, v252, 1, v247
	v_add_u32_e32 v253, 128, v244
	v_xor_b32_e32 v253, v253, v254
	v_lshl_add_u32 v253, v253, 1, v247
	v_fma_mixlo_f16 v82, v82, v232, 0
	v_fma_mixlo_f16 v84, v84, v232, 0
	v_fma_mixlo_f16 v86, v86, v232, 0
	v_fma_mixlo_f16 v88, v88, v232, 0
	v_fma_mixhi_f16 v82, v83, v232, 0
	v_fma_mixhi_f16 v84, v85, v232, 0
	v_fma_mixhi_f16 v86, v87, v232, 0
	v_fma_mixhi_f16 v88, v89, v232, 0
	v_cndmask_b32_e64 v83, v82, v84, s[12:13]
	v_cndmask_b32_e64 v85, v84, v82, s[12:13]
	v_cndmask_b32_e64 v87, v86, v88, s[12:13]
	v_cndmask_b32_e64 v89, v88, v86, s[12:13]
	v_mov_b32_e32 v254, v248
	v_add_u32_e32 v247, 0x1800, v248
	v_mov_b32_dpp v244, v83 quad_perm:[1,0,3,2] row_mask:0xf bank_mask:0xf
	v_mov_b32_dpp v255, v87 quad_perm:[1,0,3,2] row_mask:0xf bank_mask:0xf
	v_perm_b32 v82, v244, v85, v245
	v_perm_b32 v84, v244, v85, v246
	ds_write2_b32 v254, v82, v84 offset1:96
	v_perm_b32 v86, v255, v89, v245
	v_perm_b32 v88, v255, v89, v246
	ds_write2_b32 v247, v86, v88 offset1:96
	v_fma_mixlo_f16 v90, v90, v232, 0
	v_fma_mixlo_f16 v92, v92, v232, 0
	v_fma_mixlo_f16 v94, v94, v232, 0
	v_fma_mixlo_f16 v96, v96, v232, 0
	v_fma_mixhi_f16 v90, v91, v232, 0
	v_fma_mixhi_f16 v92, v93, v232, 0
	v_fma_mixhi_f16 v94, v95, v232, 0
	v_fma_mixhi_f16 v96, v97, v232, 0
	v_cndmask_b32_e64 v91, v90, v92, s[12:13]
	v_cndmask_b32_e64 v93, v92, v90, s[12:13]
	v_cndmask_b32_e64 v95, v94, v96, s[12:13]
	v_cndmask_b32_e64 v97, v96, v94, s[12:13]
	v_add_u32_e32 v254, 0xc000, v248
	v_add_u32_e32 v247, 0xd800, v248
	v_mov_b32_dpp v244, v91 quad_perm:[1,0,3,2] row_mask:0xf bank_mask:0xf
	v_mov_b32_dpp v255, v95 quad_perm:[1,0,3,2] row_mask:0xf bank_mask:0xf
	v_perm_b32 v90, v244, v93, v245
	v_perm_b32 v92, v244, v93, v246
	ds_write2_b32 v254, v90, v92 offset1:96
	v_perm_b32 v94, v255, v97, v245
	v_perm_b32 v96, v255, v97, v246
	ds_write2_b32 v247, v94, v96 offset1:96
	v_fma_mixlo_f16 v70, v70, v233, 0
	v_fma_mixlo_f16 v72, v72, v233, 0
	v_fma_mixlo_f16 v66, v66, v233, 0
	v_fma_mixlo_f16 v68, v68, v233, 0
	v_fma_mixhi_f16 v70, v71, v233, 0
	v_fma_mixhi_f16 v72, v73, v233, 0
	v_fma_mixhi_f16 v66, v67, v233, 0
	v_fma_mixhi_f16 v68, v69, v233, 0
	v_cndmask_b32_e64 v71, v70, v72, s[12:13]
	v_cndmask_b32_e64 v73, v72, v70, s[12:13]
	v_cndmask_b32_e64 v67, v66, v68, s[12:13]
	v_cndmask_b32_e64 v69, v68, v66, s[12:13]
	v_mov_b32_e32 v254, v249
	v_add_u32_e32 v247, 0x1800, v249
	v_mov_b32_dpp v244, v71 quad_perm:[1,0,3,2] row_mask:0xf bank_mask:0xf
	v_mov_b32_dpp v255, v67 quad_perm:[1,0,3,2] row_mask:0xf bank_mask:0xf
	v_perm_b32 v70, v244, v73, v245
	v_perm_b32 v72, v244, v73, v246
	ds_write2_b32 v254, v70, v72 offset1:96
	v_perm_b32 v66, v255, v69, v245
	v_perm_b32 v68, v255, v69, v246
	ds_write2_b32 v247, v66, v68 offset1:96
	v_fma_mixlo_f16 v78, v78, v233, 0
	v_fma_mixlo_f16 v80, v80, v233, 0
	v_fma_mixlo_f16 v74, v74, v233, 0
	v_fma_mixlo_f16 v76, v76, v233, 0
	v_fma_mixhi_f16 v78, v79, v233, 0
	v_fma_mixhi_f16 v80, v81, v233, 0
	v_fma_mixhi_f16 v74, v75, v233, 0
	v_fma_mixhi_f16 v76, v77, v233, 0
	v_cndmask_b32_e64 v79, v78, v80, s[12:13]
	v_cndmask_b32_e64 v81, v80, v78, s[12:13]
	v_cndmask_b32_e64 v75, v74, v76, s[12:13]
	v_cndmask_b32_e64 v77, v76, v74, s[12:13]
	v_add_u32_e32 v254, 0xc000, v249
	v_add_u32_e32 v247, 0xd800, v249
	v_mov_b32_dpp v244, v79 quad_perm:[1,0,3,2] row_mask:0xf bank_mask:0xf
	v_mov_b32_dpp v255, v75 quad_perm:[1,0,3,2] row_mask:0xf bank_mask:0xf
	v_perm_b32 v78, v244, v81, v245
	v_perm_b32 v80, v244, v81, v246
	ds_write2_b32 v254, v78, v80 offset1:96
	v_perm_b32 v74, v255, v77, v245
	v_perm_b32 v76, v255, v77, v246
	ds_write2_b32 v247, v74, v76 offset1:96
	v_fma_mixlo_f16 v46, v46, v234, 0
	v_fma_mixlo_f16 v48, v48, v234, 0
	v_fma_mixlo_f16 v42, v42, v234, 0
	v_fma_mixlo_f16 v44, v44, v234, 0
	v_fma_mixhi_f16 v46, v47, v234, 0
	v_fma_mixhi_f16 v48, v49, v234, 0
	v_fma_mixhi_f16 v42, v43, v234, 0
	v_fma_mixhi_f16 v44, v45, v234, 0
	v_cndmask_b32_e64 v47, v46, v48, s[12:13]
	v_cndmask_b32_e64 v49, v48, v46, s[12:13]
	v_cndmask_b32_e64 v43, v42, v44, s[12:13]
	v_cndmask_b32_e64 v45, v44, v42, s[12:13]
	v_mov_b32_e32 v254, v250
	v_add_u32_e32 v247, 0x1800, v250
	v_mov_b32_dpp v244, v47 quad_perm:[1,0,3,2] row_mask:0xf bank_mask:0xf
	v_mov_b32_dpp v255, v43 quad_perm:[1,0,3,2] row_mask:0xf bank_mask:0xf
	v_perm_b32 v46, v244, v49, v245
	v_perm_b32 v48, v244, v49, v246
	ds_write2_b32 v254, v46, v48 offset1:96
	v_perm_b32 v42, v255, v45, v245
	v_perm_b32 v44, v255, v45, v246
	ds_write2_b32 v247, v42, v44 offset1:96
	v_fma_mixlo_f16 v62, v62, v234, 0
	v_fma_mixlo_f16 v64, v64, v234, 0
	v_fma_mixlo_f16 v58, v58, v234, 0
	v_fma_mixlo_f16 v60, v60, v234, 0
	v_fma_mixhi_f16 v62, v63, v234, 0
	v_fma_mixhi_f16 v64, v65, v234, 0
	v_fma_mixhi_f16 v58, v59, v234, 0
	v_fma_mixhi_f16 v60, v61, v234, 0
	v_cndmask_b32_e64 v63, v62, v64, s[12:13]
	v_cndmask_b32_e64 v65, v64, v62, s[12:13]
	v_cndmask_b32_e64 v59, v58, v60, s[12:13]
	v_cndmask_b32_e64 v61, v60, v58, s[12:13]
	v_add_u32_e32 v254, 0xc000, v250
	v_add_u32_e32 v247, 0xd800, v250
	v_mov_b32_dpp v244, v63 quad_perm:[1,0,3,2] row_mask:0xf bank_mask:0xf
	v_mov_b32_dpp v255, v59 quad_perm:[1,0,3,2] row_mask:0xf bank_mask:0xf
	v_perm_b32 v62, v244, v65, v245
	v_perm_b32 v64, v244, v65, v246
	ds_write2_b32 v254, v62, v64 offset1:96
	v_perm_b32 v58, v255, v61, v245
	v_perm_b32 v60, v255, v61, v246
	ds_write2_b32 v247, v58, v60 offset1:96
	v_fma_mixlo_f16 v38, v38, v235, 0
	v_fma_mixlo_f16 v40, v40, v235, 0
	v_fma_mixlo_f16 v34, v34, v235, 0
	v_fma_mixlo_f16 v36, v36, v235, 0
	v_fma_mixhi_f16 v38, v39, v235, 0
	v_fma_mixhi_f16 v40, v41, v235, 0
	v_fma_mixhi_f16 v34, v35, v235, 0
	v_fma_mixhi_f16 v36, v37, v235, 0
	v_cndmask_b32_e64 v39, v38, v40, s[12:13]
	v_cndmask_b32_e64 v41, v40, v38, s[12:13]
	v_cndmask_b32_e64 v35, v34, v36, s[12:13]
	v_cndmask_b32_e64 v37, v36, v34, s[12:13]
	v_mov_b32_e32 v254, v251
	v_add_u32_e32 v247, 0x1800, v251
	v_mov_b32_dpp v244, v39 quad_perm:[1,0,3,2] row_mask:0xf bank_mask:0xf
	v_mov_b32_dpp v255, v35 quad_perm:[1,0,3,2] row_mask:0xf bank_mask:0xf
	v_perm_b32 v38, v244, v41, v245
	v_perm_b32 v40, v244, v41, v246
	ds_write2_b32 v254, v38, v40 offset1:96
	v_perm_b32 v34, v255, v37, v245
	v_perm_b32 v36, v255, v37, v246
	ds_write2_b32 v247, v34, v36 offset1:96
	v_fma_mixlo_f16 v54, v54, v235, 0
	v_fma_mixlo_f16 v56, v56, v235, 0
	v_fma_mixlo_f16 v50, v50, v235, 0
	v_fma_mixlo_f16 v52, v52, v235, 0
	v_fma_mixhi_f16 v54, v55, v235, 0
	v_fma_mixhi_f16 v56, v57, v235, 0
	v_fma_mixhi_f16 v50, v51, v235, 0
	v_fma_mixhi_f16 v52, v53, v235, 0
	v_cndmask_b32_e64 v55, v54, v56, s[12:13]
	v_cndmask_b32_e64 v57, v56, v54, s[12:13]
	v_cndmask_b32_e64 v51, v50, v52, s[12:13]
	v_cndmask_b32_e64 v53, v52, v50, s[12:13]
	v_add_u32_e32 v254, 0xc000, v251
	v_add_u32_e32 v247, 0xd800, v251
	v_mov_b32_dpp v244, v55 quad_perm:[1,0,3,2] row_mask:0xf bank_mask:0xf
	v_mov_b32_dpp v255, v51 quad_perm:[1,0,3,2] row_mask:0xf bank_mask:0xf
	v_perm_b32 v54, v244, v57, v245
	v_perm_b32 v56, v244, v57, v246
	ds_write2_b32 v254, v54, v56 offset1:96
	v_perm_b32 v50, v255, v53, v245
	v_perm_b32 v52, v255, v53, v246
	ds_write2_b32 v247, v50, v52 offset1:96
	v_fma_mixlo_f16 v22, v22, v236, 0
	v_fma_mixlo_f16 v24, v24, v236, 0
	v_fma_mixlo_f16 v18, v18, v236, 0
	v_fma_mixlo_f16 v20, v20, v236, 0
	v_fma_mixhi_f16 v22, v23, v236, 0
	v_fma_mixhi_f16 v24, v25, v236, 0
	v_fma_mixhi_f16 v18, v19, v236, 0
	v_fma_mixhi_f16 v20, v21, v236, 0
	v_cndmask_b32_e64 v23, v22, v24, s[12:13]
	v_cndmask_b32_e64 v25, v24, v22, s[12:13]
	v_cndmask_b32_e64 v19, v18, v20, s[12:13]
	v_cndmask_b32_e64 v21, v20, v18, s[12:13]
	v_mov_b32_e32 v254, v252
	v_add_u32_e32 v247, 0x1800, v252
	v_mov_b32_dpp v244, v23 quad_perm:[1,0,3,2] row_mask:0xf bank_mask:0xf
	v_mov_b32_dpp v255, v19 quad_perm:[1,0,3,2] row_mask:0xf bank_mask:0xf
	v_perm_b32 v22, v244, v25, v245
	v_perm_b32 v24, v244, v25, v246
	ds_write2_b32 v254, v22, v24 offset1:96
	v_perm_b32 v18, v255, v21, v245
	v_perm_b32 v20, v255, v21, v246
	ds_write2_b32 v247, v18, v20 offset1:96
	v_fma_mixlo_f16 v30, v30, v236, 0
	v_fma_mixlo_f16 v32, v32, v236, 0
	v_fma_mixlo_f16 v26, v26, v236, 0
	v_fma_mixlo_f16 v28, v28, v236, 0
	v_fma_mixhi_f16 v30, v31, v236, 0
	v_fma_mixhi_f16 v32, v33, v236, 0
	v_fma_mixhi_f16 v26, v27, v236, 0
	v_fma_mixhi_f16 v28, v29, v236, 0
	v_cndmask_b32_e64 v31, v30, v32, s[12:13]
	v_cndmask_b32_e64 v33, v32, v30, s[12:13]
	v_cndmask_b32_e64 v27, v26, v28, s[12:13]
	v_cndmask_b32_e64 v29, v28, v26, s[12:13]
	v_add_u32_e32 v254, 0xc000, v252
	v_add_u32_e32 v247, 0xd800, v252
	v_mov_b32_dpp v244, v31 quad_perm:[1,0,3,2] row_mask:0xf bank_mask:0xf
	v_mov_b32_dpp v255, v27 quad_perm:[1,0,3,2] row_mask:0xf bank_mask:0xf
	v_perm_b32 v30, v244, v33, v245
	v_perm_b32 v32, v244, v33, v246
	ds_write2_b32 v254, v30, v32 offset1:96
	v_perm_b32 v26, v255, v29, v245
	v_perm_b32 v28, v255, v29, v246
	ds_write2_b32 v247, v26, v28 offset1:96
	v_fma_mixlo_f16 v6, v6, v237, 0
	v_fma_mixlo_f16 v8, v8, v237, 0
	v_fma_mixlo_f16 v2, v2, v237, 0
	v_fma_mixlo_f16 v4, v4, v237, 0
	v_fma_mixhi_f16 v6, v7, v237, 0
	v_fma_mixhi_f16 v8, v9, v237, 0
	v_fma_mixhi_f16 v2, v3, v237, 0
	v_fma_mixhi_f16 v4, v5, v237, 0
	v_cndmask_b32_e64 v7, v6, v8, s[12:13]
	v_cndmask_b32_e64 v9, v8, v6, s[12:13]
	v_cndmask_b32_e64 v3, v2, v4, s[12:13]
	v_cndmask_b32_e64 v5, v4, v2, s[12:13]
	v_mov_b32_e32 v254, v253
	v_add_u32_e32 v247, 0x1800, v253
	v_mov_b32_dpp v244, v7 quad_perm:[1,0,3,2] row_mask:0xf bank_mask:0xf
	v_mov_b32_dpp v255, v3 quad_perm:[1,0,3,2] row_mask:0xf bank_mask:0xf
	v_perm_b32 v6, v244, v9, v245
	v_perm_b32 v8, v244, v9, v246
	ds_write2_b32 v254, v6, v8 offset1:96
	v_perm_b32 v2, v255, v5, v245
	v_perm_b32 v4, v255, v5, v246
	ds_write2_b32 v247, v2, v4 offset1:96
	v_fma_mixlo_f16 v14, v14, v237, 0
	v_fma_mixlo_f16 v16, v16, v237, 0
	v_fma_mixlo_f16 v10, v10, v237, 0
	v_fma_mixlo_f16 v12, v12, v237, 0
	v_fma_mixhi_f16 v14, v15, v237, 0
	v_fma_mixhi_f16 v16, v17, v237, 0
	v_fma_mixhi_f16 v10, v11, v237, 0
	v_fma_mixhi_f16 v12, v13, v237, 0
	v_cndmask_b32_e64 v15, v14, v16, s[12:13]
	v_cndmask_b32_e64 v17, v16, v14, s[12:13]
	v_cndmask_b32_e64 v11, v10, v12, s[12:13]
	v_cndmask_b32_e64 v13, v12, v10, s[12:13]
	v_add_u32_e32 v254, 0xc000, v253
	v_add_u32_e32 v247, 0xd800, v253
	v_mov_b32_dpp v244, v15 quad_perm:[1,0,3,2] row_mask:0xf bank_mask:0xf
	v_mov_b32_dpp v255, v11 quad_perm:[1,0,3,2] row_mask:0xf bank_mask:0xf
	v_perm_b32 v14, v244, v17, v245
	v_perm_b32 v16, v244, v17, v246
	ds_write2_b32 v254, v14, v16 offset1:96
	v_perm_b32 v10, v255, v13, v245
	v_perm_b32 v12, v255, v13, v246
	ds_write2_b32 v247, v10, v12 offset1:96
	s_movk_i32 s0, 0x80
	v_cmp_gt_i32_e64 s[2:3], s1, v107
	s_waitcnt vmcnt(5)
	s_waitcnt vmcnt(4)
	v_xor_b32_e32 v66, v108, v124
	v_lshlrev_b32_e32 v66, 1, v66
	v_add3_u32 v66, 0, v66, v105
	s_waitcnt vmcnt(3)
	v_xor_b32_e32 v42, v110, v124
	v_lshlrev_b32_e32 v42, 1, v42
	v_add3_u32 v42, 0, v42, v105
	s_waitcnt vmcnt(2)
	v_xor_b32_e32 v34, v111, v124
	v_lshlrev_b32_e32 v34, 1, v34
	v_add3_u32 v34, 0, v34, v105
	s_waitcnt vmcnt(1)
	v_bitop3_b32 v18, v100, v124, s0 bitop3:0x36
	v_lshlrev_b32_e32 v18, 1, v18
	v_add3_u32 v18, 0, v18, v105
	s_waitcnt vmcnt(0)
	s_mov_b32 s0, 0x2aaaaaab
	v_mul_hi_i32 v2, v107, s0
	v_lshrrev_b32_e32 v3, 31, v2
	v_ashrrev_i32_e32 v2, 4, v2
	v_add_u32_e32 v49, v2, v3
	s_movk_i32 s0, 0x60
	v_mul_lo_u32 v2, v49, s0
	v_sub_u32_e32 v14, v107, v2
	v_lshrrev_b32_e32 v2, 1, v121
	s_movk_i32 s0, 0x5e80
	v_add_u32_e32 v8, v14, v2
	v_mov_b32_e32 v7, 0
	v_lshlrev_b32_e32 v2, 2, v14
	v_mul_lo_u32 v3, v49, s0
	v_ashrrev_i32_e32 v9, 31, v8
	v_mul_lo_u32 v45, v49, s75
	v_xor_b32_e32 v48, 0x60, v2
	v_xor_b32_e32 v47, 64, v2
	v_xor_b32_e32 v46, 32, v2
	v_add3_u32 v44, v3, v123, 0
	v_mov_b32_e32 v6, v7
	v_mov_b32_e32 v3, v7
	v_mov_b32_e32 v4, v7
	s_waitcnt lgkmcnt(0)
	s_barrier
	s_and_saveexec_b64 s[0:1], s[2:3]
	s_cbranch_execz .LBB1_73
	v_readlane_b32 s4, v230, 2
	v_readlane_b32 s5, v230, 3
	v_mov_b32_e32 v12, 0
	v_mov_b32_e32 v13, v12
	v_mov_b32_e32 v2, v240
	v_mov_b32_e32 v3, v241
	v_mov_b32_e32 v6, v242
	v_mov_b32_e32 v7, v243
	v_readlane_b32 s4, v230, 10
	v_readlane_b32 s6, v230, 4
	v_readlane_b32 s7, v230, 5
	v_add3_u32 v15, v45, v48, s4
	s_add_i32 s4, 0, 0xc00
	v_add3_u32 v16, v45, v47, s4
	s_add_i32 s4, 0, 0x600
	v_add3_u32 v17, v45, v46, s4
	v_mov_b32_e32 v26, v44
	v_add_u32_e32 v27, 0x200, v44
	v_mov_b32_e32 v28, v17
	v_add_u32_e32 v29, 0x200, v17
	v_mov_b32_e32 v30, v16
	v_add_u32_e32 v31, 0x200, v16
	v_mov_b32_e32 v32, v15
	v_add_u32_e32 v33, 0x200, v15
	ds_read2_b32 v[50:51], v26 offset1:96
	ds_read2_b32 v[52:53], v27 offset0:64 offset1:160
	ds_read2_b32 v[54:55], v28 offset1:96
	ds_read2_b32 v[56:57], v29 offset0:64 offset1:160
	v_add_u32_e32 v26, 0x1800, v26
	v_add_u32_e32 v27, 0x1800, v27
	v_add_u32_e32 v28, 0x1800, v28
	v_add_u32_e32 v29, 0x1800, v29
	ds_read2_b32 v[58:59], v30 offset1:96
	ds_read2_b32 v[60:61], v31 offset0:64 offset1:160
	ds_read2_b32 v[62:63], v32 offset1:96
	ds_read2_b32 v[64:65], v33 offset0:64 offset1:160
	v_add_u32_e32 v30, 0x1800, v30
	v_add_u32_e32 v31, 0x1800, v31
	v_add_u32_e32 v32, 0x1800, v32
	v_add_u32_e32 v33, 0x1800, v33
	ds_read2_b32 v[66:67], v26 offset1:96
	ds_read2_b32 v[68:69], v27 offset0:64 offset1:160
	ds_read2_b32 v[70:71], v28 offset1:96
	ds_read2_b32 v[72:73], v29 offset0:64 offset1:160
	v_add_u32_e32 v26, 0x1800, v26
	v_add_u32_e32 v27, 0x1800, v27
	v_add_u32_e32 v28, 0x1800, v28
	v_add_u32_e32 v29, 0x1800, v29
	s_waitcnt vmcnt(1)
	v_xor_b32_e32 v4, 0x80000000, v3
	v_mov_b32_e32 v10, v2
	v_mov_b32_e32 v11, v2
	v_mov_b32_e32 v5, v3
	s_waitcnt lgkmcnt(8)
	v_cvt_f32_f16_e32 v74, v50
	v_cvt_f32_f16_sdwa v75, v50 dst_sel:DWORD dst_unused:UNUSED_PAD src0_sel:WORD_1
	v_cvt_f32_f16_e32 v76, v51
	v_cvt_f32_f16_sdwa v77, v51 dst_sel:DWORD dst_unused:UNUSED_PAD src0_sel:WORD_1
	v_cvt_f32_f16_e32 v78, v52
	v_cvt_f32_f16_sdwa v79, v52 dst_sel:DWORD dst_unused:UNUSED_PAD src0_sel:WORD_1
	v_cvt_f32_f16_e32 v80, v53
	v_cvt_f32_f16_sdwa v81, v53 dst_sel:DWORD dst_unused:UNUSED_PAD src0_sel:WORD_1
	v_cvt_f32_f16_e32 v82, v54
	v_cvt_f32_f16_sdwa v83, v54 dst_sel:DWORD dst_unused:UNUSED_PAD src0_sel:WORD_1
	v_cvt_f32_f16_e32 v84, v55
	v_cvt_f32_f16_sdwa v85, v55 dst_sel:DWORD dst_unused:UNUSED_PAD src0_sel:WORD_1
	v_cvt_f32_f16_e32 v86, v56
	v_cvt_f32_f16_sdwa v87, v56 dst_sel:DWORD dst_unused:UNUSED_PAD src0_sel:WORD_1
	v_cvt_f32_f16_e32 v88, v57
	v_cvt_f32_f16_sdwa v89, v57 dst_sel:DWORD dst_unused:UNUSED_PAD src0_sel:WORD_1
	ds_read2_b32 v[50:51], v30 offset1:96
	ds_read2_b32 v[52:53], v31 offset0:64 offset1:160
	ds_read2_b32 v[54:55], v32 offset1:96
	ds_read2_b32 v[56:57], v33 offset0:64 offset1:160
	v_add_u32_e32 v30, 0x1800, v30
	v_add_u32_e32 v31, 0x1800, v31
	v_add_u32_e32 v32, 0x1800, v32
	v_add_u32_e32 v33, 0x1800, v33
	s_waitcnt lgkmcnt(8)
	v_pk_fma_f32 v[74:75], v[4:5], v[12:13], v[74:75] op_sel:[0,1,0] op_sel_hi:[1,0,1]
	v_cvt_f32_f16_e32 v90, v58
	v_pk_fma_f32 v[12:13], v[10:11], v[12:13], v[74:75]
	v_cvt_f32_f16_sdwa v91, v58 dst_sel:DWORD dst_unused:UNUSED_PAD src0_sel:WORD_1
	v_pk_fma_f32 v[76:77], v[4:5], v[12:13], v[76:77] op_sel:[0,1,0] op_sel_hi:[1,0,1]
	v_cvt_f32_f16_e32 v92, v59
	v_pk_fma_f32 v[12:13], v[10:11], v[12:13], v[76:77]
	v_cvt_f32_f16_sdwa v93, v59 dst_sel:DWORD dst_unused:UNUSED_PAD src0_sel:WORD_1
	v_pk_fma_f32 v[78:79], v[4:5], v[12:13], v[78:79] op_sel:[0,1,0] op_sel_hi:[1,0,1]
	v_cvt_f32_f16_e32 v94, v60
	v_pk_fma_f32 v[12:13], v[10:11], v[12:13], v[78:79]
	v_cvt_f32_f16_sdwa v95, v60 dst_sel:DWORD dst_unused:UNUSED_PAD src0_sel:WORD_1
	v_pk_fma_f32 v[80:81], v[4:5], v[12:13], v[80:81] op_sel:[0,1,0] op_sel_hi:[1,0,1]
	v_cvt_f32_f16_e32 v96, v61
	v_pk_fma_f32 v[12:13], v[10:11], v[12:13], v[80:81]
	v_cvt_f32_f16_sdwa v97, v61 dst_sel:DWORD dst_unused:UNUSED_PAD src0_sel:WORD_1
	v_pk_fma_f32 v[82:83], v[4:5], v[12:13], v[82:83] op_sel:[0,1,0] op_sel_hi:[1,0,1]
	v_cvt_f32_f16_e32 v18, v62
	v_pk_fma_f32 v[12:13], v[10:11], v[12:13], v[82:83]
	v_cvt_f32_f16_sdwa v19, v62 dst_sel:DWORD dst_unused:UNUSED_PAD src0_sel:WORD_1
	v_pk_fma_f32 v[84:85], v[4:5], v[12:13], v[84:85] op_sel:[0,1,0] op_sel_hi:[1,0,1]
	v_cvt_f32_f16_e32 v20, v63
	v_pk_fma_f32 v[12:13], v[10:11], v[12:13], v[84:85]
	v_cvt_f32_f16_sdwa v21, v63 dst_sel:DWORD dst_unused:UNUSED_PAD src0_sel:WORD_1
	v_pk_fma_f32 v[86:87], v[4:5], v[12:13], v[86:87] op_sel:[0,1,0] op_sel_hi:[1,0,1]
	v_cvt_f32_f16_e32 v22, v64
	v_pk_fma_f32 v[12:13], v[10:11], v[12:13], v[86:87]
	v_cvt_f32_f16_sdwa v23, v64 dst_sel:DWORD dst_unused:UNUSED_PAD src0_sel:WORD_1
	v_pk_fma_f32 v[88:89], v[4:5], v[12:13], v[88:89] op_sel:[0,1,0] op_sel_hi:[1,0,1]
	v_cvt_f32_f16_e32 v24, v65
	v_pk_fma_f32 v[12:13], v[10:11], v[12:13], v[88:89]
	v_cvt_f32_f16_sdwa v25, v65 dst_sel:DWORD dst_unused:UNUSED_PAD src0_sel:WORD_1
	ds_read2_b32 v[58:59], v26 offset1:96
	ds_read2_b32 v[60:61], v27 offset0:64 offset1:160
	ds_read2_b32 v[62:63], v28 offset1:96
	ds_read2_b32 v[64:65], v29 offset0:64 offset1:160
	v_add_u32_e32 v26, 0x1800, v26
	v_add_u32_e32 v27, 0x1800, v27
	v_add_u32_e32 v28, 0x1800, v28
	v_add_u32_e32 v29, 0x1800, v29
	s_waitcnt lgkmcnt(8)
	v_pk_fma_f32 v[90:91], v[4:5], v[12:13], v[90:91] op_sel:[0,1,0] op_sel_hi:[1,0,1]
	v_cvt_f32_f16_e32 v74, v66
	v_pk_fma_f32 v[12:13], v[10:11], v[12:13], v[90:91]
	v_cvt_f32_f16_sdwa v75, v66 dst_sel:DWORD dst_unused:UNUSED_PAD src0_sel:WORD_1
	v_pk_fma_f32 v[92:93], v[4:5], v[12:13], v[92:93] op_sel:[0,1,0] op_sel_hi:[1,0,1]
	v_cvt_f32_f16_e32 v76, v67
	v_pk_fma_f32 v[12:13], v[10:11], v[12:13], v[92:93]
	v_cvt_f32_f16_sdwa v77, v67 dst_sel:DWORD dst_unused:UNUSED_PAD src0_sel:WORD_1
	v_pk_fma_f32 v[94:95], v[4:5], v[12:13], v[94:95] op_sel:[0,1,0] op_sel_hi:[1,0,1]
	v_cvt_f32_f16_e32 v78, v68
	v_pk_fma_f32 v[12:13], v[10:11], v[12:13], v[94:95]
	v_cvt_f32_f16_sdwa v79, v68 dst_sel:DWORD dst_unused:UNUSED_PAD src0_sel:WORD_1
	v_pk_fma_f32 v[96:97], v[4:5], v[12:13], v[96:97] op_sel:[0,1,0] op_sel_hi:[1,0,1]
	v_cvt_f32_f16_e32 v80, v69
	v_pk_fma_f32 v[12:13], v[10:11], v[12:13], v[96:97]
	v_cvt_f32_f16_sdwa v81, v69 dst_sel:DWORD dst_unused:UNUSED_PAD src0_sel:WORD_1
	v_pk_fma_f32 v[18:19], v[4:5], v[12:13], v[18:19] op_sel:[0,1,0] op_sel_hi:[1,0,1]
	v_cvt_f32_f16_e32 v82, v70
	v_pk_fma_f32 v[12:13], v[10:11], v[12:13], v[18:19]
	v_cvt_f32_f16_sdwa v83, v70 dst_sel:DWORD dst_unused:UNUSED_PAD src0_sel:WORD_1
	v_pk_fma_f32 v[20:21], v[4:5], v[12:13], v[20:21] op_sel:[0,1,0] op_sel_hi:[1,0,1]
	v_cvt_f32_f16_e32 v84, v71
	v_pk_fma_f32 v[12:13], v[10:11], v[12:13], v[20:21]
	v_cvt_f32_f16_sdwa v85, v71 dst_sel:DWORD dst_unused:UNUSED_PAD src0_sel:WORD_1
	v_pk_fma_f32 v[22:23], v[4:5], v[12:13], v[22:23] op_sel:[0,1,0] op_sel_hi:[1,0,1]
	v_cvt_f32_f16_e32 v86, v72
	v_pk_fma_f32 v[12:13], v[10:11], v[12:13], v[22:23]
	v_cvt_f32_f16_sdwa v87, v72 dst_sel:DWORD dst_unused:UNUSED_PAD src0_sel:WORD_1
	v_pk_fma_f32 v[24:25], v[4:5], v[12:13], v[24:25] op_sel:[0,1,0] op_sel_hi:[1,0,1]
	v_cvt_f32_f16_e32 v88, v73
	v_pk_fma_f32 v[12:13], v[10:11], v[12:13], v[24:25]
	v_cvt_f32_f16_sdwa v89, v73 dst_sel:DWORD dst_unused:UNUSED_PAD src0_sel:WORD_1
	ds_read2_b32 v[66:67], v30 offset1:96
	ds_read2_b32 v[68:69], v31 offset0:64 offset1:160
	ds_read2_b32 v[70:71], v32 offset1:96
	ds_read2_b32 v[72:73], v33 offset0:64 offset1:160
	v_add_u32_e32 v30, 0x1800, v30
	v_add_u32_e32 v31, 0x1800, v31
	v_add_u32_e32 v32, 0x1800, v32
	v_add_u32_e32 v33, 0x1800, v33
	s_waitcnt lgkmcnt(8)
	v_pk_fma_f32 v[74:75], v[4:5], v[12:13], v[74:75] op_sel:[0,1,0] op_sel_hi:[1,0,1]
	v_cvt_f32_f16_e32 v90, v50
	v_pk_fma_f32 v[12:13], v[10:11], v[12:13], v[74:75]
	v_cvt_f32_f16_sdwa v91, v50 dst_sel:DWORD dst_unused:UNUSED_PAD src0_sel:WORD_1
	v_pk_fma_f32 v[76:77], v[4:5], v[12:13], v[76:77] op_sel:[0,1,0] op_sel_hi:[1,0,1]
	v_cvt_f32_f16_e32 v92, v51
	v_pk_fma_f32 v[12:13], v[10:11], v[12:13], v[76:77]
	v_cvt_f32_f16_sdwa v93, v51 dst_sel:DWORD dst_unused:UNUSED_PAD src0_sel:WORD_1
	v_pk_fma_f32 v[78:79], v[4:5], v[12:13], v[78:79] op_sel:[0,1,0] op_sel_hi:[1,0,1]
	v_cvt_f32_f16_e32 v94, v52
	v_pk_fma_f32 v[12:13], v[10:11], v[12:13], v[78:79]
	v_cvt_f32_f16_sdwa v95, v52 dst_sel:DWORD dst_unused:UNUSED_PAD src0_sel:WORD_1
	v_pk_fma_f32 v[80:81], v[4:5], v[12:13], v[80:81] op_sel:[0,1,0] op_sel_hi:[1,0,1]
	v_cvt_f32_f16_e32 v96, v53
	v_pk_fma_f32 v[12:13], v[10:11], v[12:13], v[80:81]
	v_cvt_f32_f16_sdwa v97, v53 dst_sel:DWORD dst_unused:UNUSED_PAD src0_sel:WORD_1
	v_pk_fma_f32 v[82:83], v[4:5], v[12:13], v[82:83] op_sel:[0,1,0] op_sel_hi:[1,0,1]
	v_cvt_f32_f16_e32 v18, v54
	v_pk_fma_f32 v[12:13], v[10:11], v[12:13], v[82:83]
	v_cvt_f32_f16_sdwa v19, v54 dst_sel:DWORD dst_unused:UNUSED_PAD src0_sel:WORD_1
	v_pk_fma_f32 v[84:85], v[4:5], v[12:13], v[84:85] op_sel:[0,1,0] op_sel_hi:[1,0,1]
	v_cvt_f32_f16_e32 v20, v55
	v_pk_fma_f32 v[12:13], v[10:11], v[12:13], v[84:85]
	v_cvt_f32_f16_sdwa v21, v55 dst_sel:DWORD dst_unused:UNUSED_PAD src0_sel:WORD_1
	v_pk_fma_f32 v[86:87], v[4:5], v[12:13], v[86:87] op_sel:[0,1,0] op_sel_hi:[1,0,1]
	v_cvt_f32_f16_e32 v22, v56
	v_pk_fma_f32 v[12:13], v[10:11], v[12:13], v[86:87]
	v_cvt_f32_f16_sdwa v23, v56 dst_sel:DWORD dst_unused:UNUSED_PAD src0_sel:WORD_1
	v_pk_fma_f32 v[88:89], v[4:5], v[12:13], v[88:89] op_sel:[0,1,0] op_sel_hi:[1,0,1]
	v_cvt_f32_f16_e32 v24, v57
	v_pk_fma_f32 v[12:13], v[10:11], v[12:13], v[88:89]
	v_cvt_f32_f16_sdwa v25, v57 dst_sel:DWORD dst_unused:UNUSED_PAD src0_sel:WORD_1
	ds_read2_b32 v[50:51], v26 offset1:96
	ds_read2_b32 v[52:53], v27 offset0:64 offset1:160
	ds_read2_b32 v[54:55], v28 offset1:96
	ds_read2_b32 v[56:57], v29 offset0:64 offset1:160
	v_add_u32_e32 v26, 0x1800, v26
	v_add_u32_e32 v27, 0x1800, v27
	v_add_u32_e32 v28, 0x1800, v28
	v_add_u32_e32 v29, 0x1800, v29
	s_waitcnt lgkmcnt(8)
	v_pk_fma_f32 v[90:91], v[4:5], v[12:13], v[90:91] op_sel:[0,1,0] op_sel_hi:[1,0,1]
	v_cvt_f32_f16_e32 v74, v58
	v_pk_fma_f32 v[12:13], v[10:11], v[12:13], v[90:91]
	v_cvt_f32_f16_sdwa v75, v58 dst_sel:DWORD dst_unused:UNUSED_PAD src0_sel:WORD_1
	v_pk_fma_f32 v[92:93], v[4:5], v[12:13], v[92:93] op_sel:[0,1,0] op_sel_hi:[1,0,1]
	v_cvt_f32_f16_e32 v76, v59
	v_pk_fma_f32 v[12:13], v[10:11], v[12:13], v[92:93]
	v_cvt_f32_f16_sdwa v77, v59 dst_sel:DWORD dst_unused:UNUSED_PAD src0_sel:WORD_1
	v_pk_fma_f32 v[94:95], v[4:5], v[12:13], v[94:95] op_sel:[0,1,0] op_sel_hi:[1,0,1]
	v_cvt_f32_f16_e32 v78, v60
	v_pk_fma_f32 v[12:13], v[10:11], v[12:13], v[94:95]
	v_cvt_f32_f16_sdwa v79, v60 dst_sel:DWORD dst_unused:UNUSED_PAD src0_sel:WORD_1
	v_pk_fma_f32 v[96:97], v[4:5], v[12:13], v[96:97] op_sel:[0,1,0] op_sel_hi:[1,0,1]
	v_cvt_f32_f16_e32 v80, v61
	v_pk_fma_f32 v[12:13], v[10:11], v[12:13], v[96:97]
	v_cvt_f32_f16_sdwa v81, v61 dst_sel:DWORD dst_unused:UNUSED_PAD src0_sel:WORD_1
	v_pk_fma_f32 v[18:19], v[4:5], v[12:13], v[18:19] op_sel:[0,1,0] op_sel_hi:[1,0,1]
	v_cvt_f32_f16_e32 v82, v62
	v_pk_fma_f32 v[12:13], v[10:11], v[12:13], v[18:19]
	v_cvt_f32_f16_sdwa v83, v62 dst_sel:DWORD dst_unused:UNUSED_PAD src0_sel:WORD_1
	v_pk_fma_f32 v[20:21], v[4:5], v[12:13], v[20:21] op_sel:[0,1,0] op_sel_hi:[1,0,1]
	v_cvt_f32_f16_e32 v84, v63
	v_pk_fma_f32 v[12:13], v[10:11], v[12:13], v[20:21]
	v_cvt_f32_f16_sdwa v85, v63 dst_sel:DWORD dst_unused:UNUSED_PAD src0_sel:WORD_1
	v_pk_fma_f32 v[22:23], v[4:5], v[12:13], v[22:23] op_sel:[0,1,0] op_sel_hi:[1,0,1]
	v_cvt_f32_f16_e32 v86, v64
	v_pk_fma_f32 v[12:13], v[10:11], v[12:13], v[22:23]
	v_cvt_f32_f16_sdwa v87, v64 dst_sel:DWORD dst_unused:UNUSED_PAD src0_sel:WORD_1
	v_pk_fma_f32 v[24:25], v[4:5], v[12:13], v[24:25] op_sel:[0,1,0] op_sel_hi:[1,0,1]
	v_cvt_f32_f16_e32 v88, v65
	v_pk_fma_f32 v[12:13], v[10:11], v[12:13], v[24:25]
	v_cvt_f32_f16_sdwa v89, v65 dst_sel:DWORD dst_unused:UNUSED_PAD src0_sel:WORD_1
	ds_read2_b32 v[58:59], v30 offset1:96
	ds_read2_b32 v[60:61], v31 offset0:64 offset1:160
	ds_read2_b32 v[62:63], v32 offset1:96
	ds_read2_b32 v[64:65], v33 offset0:64 offset1:160
	v_add_u32_e32 v30, 0x1800, v30
	v_add_u32_e32 v31, 0x1800, v31
	v_add_u32_e32 v32, 0x1800, v32
	v_add_u32_e32 v33, 0x1800, v33
	s_waitcnt lgkmcnt(8)
	v_pk_fma_f32 v[74:75], v[4:5], v[12:13], v[74:75] op_sel:[0,1,0] op_sel_hi:[1,0,1]
	v_cvt_f32_f16_e32 v90, v66
	v_pk_fma_f32 v[12:13], v[10:11], v[12:13], v[74:75]
	v_cvt_f32_f16_sdwa v91, v66 dst_sel:DWORD dst_unused:UNUSED_PAD src0_sel:WORD_1
	v_pk_fma_f32 v[76:77], v[4:5], v[12:13], v[76:77] op_sel:[0,1,0] op_sel_hi:[1,0,1]
	v_cvt_f32_f16_e32 v92, v67
	v_pk_fma_f32 v[12:13], v[10:11], v[12:13], v[76:77]
	v_cvt_f32_f16_sdwa v93, v67 dst_sel:DWORD dst_unused:UNUSED_PAD src0_sel:WORD_1
	v_pk_fma_f32 v[78:79], v[4:5], v[12:13], v[78:79] op_sel:[0,1,0] op_sel_hi:[1,0,1]
	v_cvt_f32_f16_e32 v94, v68
	v_pk_fma_f32 v[12:13], v[10:11], v[12:13], v[78:79]
	v_cvt_f32_f16_sdwa v95, v68 dst_sel:DWORD dst_unused:UNUSED_PAD src0_sel:WORD_1
	v_pk_fma_f32 v[80:81], v[4:5], v[12:13], v[80:81] op_sel:[0,1,0] op_sel_hi:[1,0,1]
	v_cvt_f32_f16_e32 v96, v69
	v_pk_fma_f32 v[12:13], v[10:11], v[12:13], v[80:81]
	v_cvt_f32_f16_sdwa v97, v69 dst_sel:DWORD dst_unused:UNUSED_PAD src0_sel:WORD_1
	v_pk_fma_f32 v[82:83], v[4:5], v[12:13], v[82:83] op_sel:[0,1,0] op_sel_hi:[1,0,1]
	v_cvt_f32_f16_e32 v18, v70
	v_pk_fma_f32 v[12:13], v[10:11], v[12:13], v[82:83]
	v_cvt_f32_f16_sdwa v19, v70 dst_sel:DWORD dst_unused:UNUSED_PAD src0_sel:WORD_1
	v_pk_fma_f32 v[84:85], v[4:5], v[12:13], v[84:85] op_sel:[0,1,0] op_sel_hi:[1,0,1]
	v_cvt_f32_f16_e32 v20, v71
	v_pk_fma_f32 v[12:13], v[10:11], v[12:13], v[84:85]
	v_cvt_f32_f16_sdwa v21, v71 dst_sel:DWORD dst_unused:UNUSED_PAD src0_sel:WORD_1
	v_pk_fma_f32 v[86:87], v[4:5], v[12:13], v[86:87] op_sel:[0,1,0] op_sel_hi:[1,0,1]
	v_cvt_f32_f16_e32 v22, v72
	v_pk_fma_f32 v[12:13], v[10:11], v[12:13], v[86:87]
	v_cvt_f32_f16_sdwa v23, v72 dst_sel:DWORD dst_unused:UNUSED_PAD src0_sel:WORD_1
	v_pk_fma_f32 v[88:89], v[4:5], v[12:13], v[88:89] op_sel:[0,1,0] op_sel_hi:[1,0,1]
	v_cvt_f32_f16_e32 v24, v73
	v_pk_fma_f32 v[12:13], v[10:11], v[12:13], v[88:89]
	v_cvt_f32_f16_sdwa v25, v73 dst_sel:DWORD dst_unused:UNUSED_PAD src0_sel:WORD_1
	s_waitcnt lgkmcnt(4)
	v_pk_fma_f32 v[90:91], v[4:5], v[12:13], v[90:91] op_sel:[0,1,0] op_sel_hi:[1,0,1]
	v_cvt_f32_f16_e32 v74, v50
	v_pk_fma_f32 v[12:13], v[10:11], v[12:13], v[90:91]
	v_cvt_f32_f16_sdwa v75, v50 dst_sel:DWORD dst_unused:UNUSED_PAD src0_sel:WORD_1
	v_pk_fma_f32 v[92:93], v[4:5], v[12:13], v[92:93] op_sel:[0,1,0] op_sel_hi:[1,0,1]
	v_cvt_f32_f16_e32 v76, v51
	v_pk_fma_f32 v[12:13], v[10:11], v[12:13], v[92:93]
	v_cvt_f32_f16_sdwa v77, v51 dst_sel:DWORD dst_unused:UNUSED_PAD src0_sel:WORD_1
	v_pk_fma_f32 v[94:95], v[4:5], v[12:13], v[94:95] op_sel:[0,1,0] op_sel_hi:[1,0,1]
	v_cvt_f32_f16_e32 v78, v52
	v_pk_fma_f32 v[12:13], v[10:11], v[12:13], v[94:95]
	v_cvt_f32_f16_sdwa v79, v52 dst_sel:DWORD dst_unused:UNUSED_PAD src0_sel:WORD_1
	v_pk_fma_f32 v[96:97], v[4:5], v[12:13], v[96:97] op_sel:[0,1,0] op_sel_hi:[1,0,1]
	v_cvt_f32_f16_e32 v80, v53
	v_pk_fma_f32 v[12:13], v[10:11], v[12:13], v[96:97]
	v_cvt_f32_f16_sdwa v81, v53 dst_sel:DWORD dst_unused:UNUSED_PAD src0_sel:WORD_1
	v_pk_fma_f32 v[18:19], v[4:5], v[12:13], v[18:19] op_sel:[0,1,0] op_sel_hi:[1,0,1]
	v_cvt_f32_f16_e32 v82, v54
	v_pk_fma_f32 v[12:13], v[10:11], v[12:13], v[18:19]
	v_cvt_f32_f16_sdwa v83, v54 dst_sel:DWORD dst_unused:UNUSED_PAD src0_sel:WORD_1
	v_pk_fma_f32 v[20:21], v[4:5], v[12:13], v[20:21] op_sel:[0,1,0] op_sel_hi:[1,0,1]
	v_cvt_f32_f16_e32 v84, v55
	v_pk_fma_f32 v[12:13], v[10:11], v[12:13], v[20:21]
	v_cvt_f32_f16_sdwa v85, v55 dst_sel:DWORD dst_unused:UNUSED_PAD src0_sel:WORD_1
	v_pk_fma_f32 v[22:23], v[4:5], v[12:13], v[22:23] op_sel:[0,1,0] op_sel_hi:[1,0,1]
	v_cvt_f32_f16_e32 v86, v56
	v_pk_fma_f32 v[12:13], v[10:11], v[12:13], v[22:23]
	v_cvt_f32_f16_sdwa v87, v56 dst_sel:DWORD dst_unused:UNUSED_PAD src0_sel:WORD_1
	v_pk_fma_f32 v[24:25], v[4:5], v[12:13], v[24:25] op_sel:[0,1,0] op_sel_hi:[1,0,1]
	v_cvt_f32_f16_e32 v88, v57
	v_pk_fma_f32 v[12:13], v[10:11], v[12:13], v[24:25]
	v_cvt_f32_f16_sdwa v89, v57 dst_sel:DWORD dst_unused:UNUSED_PAD src0_sel:WORD_1
	s_waitcnt lgkmcnt(0)
	v_pk_fma_f32 v[74:75], v[4:5], v[12:13], v[74:75] op_sel:[0,1,0] op_sel_hi:[1,0,1]
	v_cvt_f32_f16_e32 v90, v58
	v_pk_fma_f32 v[12:13], v[10:11], v[12:13], v[74:75]
	v_cvt_f32_f16_sdwa v91, v58 dst_sel:DWORD dst_unused:UNUSED_PAD src0_sel:WORD_1
	v_pk_fma_f32 v[76:77], v[4:5], v[12:13], v[76:77] op_sel:[0,1,0] op_sel_hi:[1,0,1]
	v_cvt_f32_f16_e32 v92, v59
	v_pk_fma_f32 v[12:13], v[10:11], v[12:13], v[76:77]
	v_cvt_f32_f16_sdwa v93, v59 dst_sel:DWORD dst_unused:UNUSED_PAD src0_sel:WORD_1
	v_pk_fma_f32 v[78:79], v[4:5], v[12:13], v[78:79] op_sel:[0,1,0] op_sel_hi:[1,0,1]
	v_cvt_f32_f16_e32 v94, v60
	v_pk_fma_f32 v[12:13], v[10:11], v[12:13], v[78:79]
	v_cvt_f32_f16_sdwa v95, v60 dst_sel:DWORD dst_unused:UNUSED_PAD src0_sel:WORD_1
	v_pk_fma_f32 v[80:81], v[4:5], v[12:13], v[80:81] op_sel:[0,1,0] op_sel_hi:[1,0,1]
	v_cvt_f32_f16_e32 v96, v61
	v_pk_fma_f32 v[12:13], v[10:11], v[12:13], v[80:81]
	v_cvt_f32_f16_sdwa v97, v61 dst_sel:DWORD dst_unused:UNUSED_PAD src0_sel:WORD_1
	v_pk_fma_f32 v[82:83], v[4:5], v[12:13], v[82:83] op_sel:[0,1,0] op_sel_hi:[1,0,1]
	v_cvt_f32_f16_e32 v18, v62
	v_pk_fma_f32 v[12:13], v[10:11], v[12:13], v[82:83]
	v_cvt_f32_f16_sdwa v19, v62 dst_sel:DWORD dst_unused:UNUSED_PAD src0_sel:WORD_1
	v_pk_fma_f32 v[84:85], v[4:5], v[12:13], v[84:85] op_sel:[0,1,0] op_sel_hi:[1,0,1]
	v_cvt_f32_f16_e32 v20, v63
	v_pk_fma_f32 v[12:13], v[10:11], v[12:13], v[84:85]
	v_cvt_f32_f16_sdwa v21, v63 dst_sel:DWORD dst_unused:UNUSED_PAD src0_sel:WORD_1
	v_pk_fma_f32 v[86:87], v[4:5], v[12:13], v[86:87] op_sel:[0,1,0] op_sel_hi:[1,0,1]
	v_cvt_f32_f16_e32 v22, v64
	v_pk_fma_f32 v[12:13], v[10:11], v[12:13], v[86:87]
	v_cvt_f32_f16_sdwa v23, v64 dst_sel:DWORD dst_unused:UNUSED_PAD src0_sel:WORD_1
	v_pk_fma_f32 v[88:89], v[4:5], v[12:13], v[88:89] op_sel:[0,1,0] op_sel_hi:[1,0,1]
	v_cvt_f32_f16_e32 v24, v65
	v_pk_fma_f32 v[12:13], v[10:11], v[12:13], v[88:89]
	v_cvt_f32_f16_sdwa v25, v65 dst_sel:DWORD dst_unused:UNUSED_PAD src0_sel:WORD_1
	v_pk_fma_f32 v[90:91], v[4:5], v[12:13], v[90:91] op_sel:[0,1,0] op_sel_hi:[1,0,1]
	s_nop 0
	v_pk_fma_f32 v[12:13], v[10:11], v[12:13], v[90:91]
	s_nop 0
	v_pk_fma_f32 v[92:93], v[4:5], v[12:13], v[92:93] op_sel:[0,1,0] op_sel_hi:[1,0,1]
	s_nop 0
	v_pk_fma_f32 v[12:13], v[10:11], v[12:13], v[92:93]
	s_nop 0
	v_pk_fma_f32 v[94:95], v[4:5], v[12:13], v[94:95] op_sel:[0,1,0] op_sel_hi:[1,0,1]
	s_nop 0
	v_pk_fma_f32 v[12:13], v[10:11], v[12:13], v[94:95]
	s_nop 0
	v_pk_fma_f32 v[96:97], v[4:5], v[12:13], v[96:97] op_sel:[0,1,0] op_sel_hi:[1,0,1]
	s_nop 0
	v_pk_fma_f32 v[12:13], v[10:11], v[12:13], v[96:97]
	s_nop 0
	v_pk_fma_f32 v[18:19], v[4:5], v[12:13], v[18:19] op_sel:[0,1,0] op_sel_hi:[1,0,1]
	s_nop 0
	v_pk_fma_f32 v[12:13], v[10:11], v[12:13], v[18:19]
	s_nop 0
	v_pk_fma_f32 v[20:21], v[4:5], v[12:13], v[20:21] op_sel:[0,1,0] op_sel_hi:[1,0,1]
	s_nop 0
	v_pk_fma_f32 v[12:13], v[10:11], v[12:13], v[20:21]
	s_nop 0
	v_pk_fma_f32 v[22:23], v[4:5], v[12:13], v[22:23] op_sel:[0,1,0] op_sel_hi:[1,0,1]
	s_nop 0
	v_pk_fma_f32 v[12:13], v[10:11], v[12:13], v[22:23]
	s_nop 0
	v_pk_fma_f32 v[24:25], v[4:5], v[12:13], v[24:25] op_sel:[0,1,0] op_sel_hi:[1,0,1]
	s_nop 0
	v_pk_fma_f32 v[12:13], v[10:11], v[12:13], v[24:25]
	s_nop 0
	v_mul_lo_u32 v4, v49, s67
	v_lshlrev_b32_e32 v5, 3, v14
	v_readlane_b32 s4, v230, 8
	s_nop 1
	v_add3_u32 v4, s4, v4, v5
	ds_write_b64 v4, v[12:13]
	v_mov_b32_e32 v4, v2
